# second epilogue sjob issued after the 7th epilogue store (was the 6th), consumed at the end of the next unit's first K-loop trip
# speedup vs baseline: 1.0241x; 1.0010x over previous
; __device__ __forceinline__ unsigned pk4_fp8(float a, float b, float c, float d) { int p = __builtin_amdgcn_cvt_pk_fp8_f32(a, b, 0, false); p = __builtin_amdgcn_cvt_pk_fp8_f32(c, d, p, true); return (unsigned)p; }
;     __device__ __forceinline__ void operator()(const f32x4 (&acc)[2][2][4][2], const Unit& u, int wr, int wc, int fr, int fq) const {
;     ...
;         for (int ai = 0; ai < 2; ++ai)
; #pragma unroll
;             for (int m = 0; m < 4; ++m) { float r[8];
; #pragma unroll
;                 for (int n = 0; n < 2; ++n)
; #pragma unroll
;                     for (int j = 0; j < 4; ++j) {
;                         float g = acc[ai][0][m][n][j] * W8_INV + bg[n][j], uu = acc[ai][1][m][n][j] * W8_INV + bu[n][j];
;                         g = fminf(g, 7.0f); uu = fminf(fmaxf(uu, -7.0f), 7.0f);
;                         const float glu = g * __builtin_amdgcn_rcpf(1.0f + __expf(-1.702f * g));
;                         r[n * 4 + j] = (uu + 1.0f) * glu; }
;                 u32x2 w; w.x = pk4_fp8(r[0], r[1], r[2], r[3]); w.y = pk4_fp8(r[4], r[5], r[6], r[7]);
;                 *(u32x2*)(O + (size_t)(row0 + ai * HALF + m * 16) * DM + cc) = w; }
.Lesj_join:
	v_fmamk_f32 v19, v175, 0x3c800000, v15
	v_fmamk_f32 v25, v166, 0x3c800000, v6
	v_min_f32_e32 v19, 0x40e00000, v19
	v_min_f32_e32 v25, 0x40e00000, v25
	v_fmamk_f32 v23, v176, 0x3c800000, v16
	v_mul_f32_e32 v36, 0xbfd9db23, v19
	v_mul_f32_e32 v39, 0xbfd9db23, v25
	v_min_f32_e32 v23, 0x40e00000, v23
	v_mul_f32_e32 v36, 0x3fb8aa3b, v36
	v_mul_f32_e32 v39, 0x3fb8aa3b, v39
	v_mul_f32_e32 v37, 0xbfd9db23, v23
	v_exp_f32_e32 v36, v36
	v_exp_f32_e32 v39, v39
	v_mul_f32_e32 v37, 0x3fb8aa3b, v37
	v_fmamk_f32 v18, v174, 0x3c800000, v14
	v_fmamk_f32 v24, v177, 0x3c800000, v17
	v_exp_f32_e32 v37, v37
	v_min_f32_e32 v18, 0x40e00000, v18
	v_min_f32_e32 v24, 0x40e00000, v24
	v_mul_f32_e32 v35, 0xbfd9db23, v18
	v_mul_f32_e32 v38, 0xbfd9db23, v24
	v_add_f32_e32 v36, 1.0, v36
	v_add_f32_e32 v39, 1.0, v39
	v_mul_f32_e32 v35, 0x3fb8aa3b, v35
	v_mul_f32_e32 v38, 0x3fb8aa3b, v38
	v_rcp_f32_e32 v36, v36
	v_rcp_f32_e32 v39, v39
	v_exp_f32_e32 v35, v35
	v_exp_f32_e32 v38, v38
	v_add_f32_e32 v37, 1.0, v37
	v_fmamk_f32 v27, v168, 0x3c800000, v8
	v_fmamk_f32 v29, v171, 0x3c800000, v11
	v_fmamk_f32 v32, v162, 0x3c800000, v2
	v_rcp_f32_e32 v37, v37
	v_min_f32_e32 v27, 0x40e00000, v27
	v_med3_f32 v29, v29, s57, v196
	v_med3_f32 v32, v32, s57, v196
	v_fmamk_f32 v26, v167, 0x3c800000, v7
	v_fmamk_f32 v30, v172, 0x3c800000, v12
	v_mul_f32_e32 v41, 0xbfd9db23, v27
	v_add_f32_e32 v29, 1.0, v29
	v_add_f32_e32 v32, 1.0, v32
	v_mul_f32_e32 v19, v19, v36
	v_mul_f32_e32 v25, v25, v39
	v_min_f32_e32 v26, 0x40e00000, v26
	v_med3_f32 v30, v30, s57, v196
	v_mul_f32_e32 v41, 0x3fb8aa3b, v41
	v_add_f32_e32 v35, 1.0, v35
	v_add_f32_e32 v38, 1.0, v38
	v_mul_f32_e32 v19, v29, v19
	v_mul_f32_e32 v29, v32, v25
	v_fmamk_f32 v25, v169, 0x3c800000, v9
	v_mul_f32_e32 v40, 0xbfd9db23, v26
	v_add_f32_e32 v30, 1.0, v30
	v_exp_f32_e32 v41, v41
	v_rcp_f32_e32 v35, v35
	v_rcp_f32_e32 v38, v38
	v_mul_f32_e32 v23, v23, v37
	v_min_f32_e32 v25, 0x40e00000, v25
	v_mul_f32_e32 v40, 0x3fb8aa3b, v40
	v_mul_f32_e32 v23, v30, v23
	v_mul_f32_e32 v30, 0xbfd9db23, v25
	v_fmamk_f32 v28, v170, 0x3c800000, v10
	v_fmamk_f32 v31, v173, 0x3c800000, v13
	v_exp_f32_e32 v40, v40
	v_mul_f32_e32 v30, 0x3fb8aa3b, v30
	v_med3_f32 v28, v28, s57, v196
	v_med3_f32 v31, v31, s57, v196
	v_exp_f32_e32 v30, v30
	v_add_f32_e32 v28, 1.0, v28
	v_add_f32_e32 v31, 1.0, v31
	v_add_f32_e32 v41, 1.0, v41
	v_mul_f32_e32 v18, v18, v35
	v_mul_f32_e32 v24, v24, v38
	v_mul_f32_e32 v18, v28, v18
	v_mul_f32_e32 v28, v31, v24
	v_rcp_f32_e32 v24, v41
	v_add_f32_e32 v40, 1.0, v40
	v_fmamk_f32 v34, v164, 0x3c800000, v4
	v_rcp_f32_e32 v40, v40
	v_add_f32_e32 v30, 1.0, v30
	v_med3_f32 v31, v34, s57, v196
	v_rcp_f32_e32 v30, v30
	v_fmamk_f32 v33, v163, 0x3c800000, v3
	v_mul_f32_e32 v24, v27, v24
	v_add_f32_e32 v27, 1.0, v31
	v_med3_f32 v33, v33, s57, v196
	v_mul_f32_e32 v27, v27, v24
	v_fmamk_f32 v24, v165, 0x3c800000, v5
	v_add_f32_e32 v33, 1.0, v33
	v_mul_f32_e32 v26, v26, v40
	v_med3_f32 v31, v24, s57, v196
	v_mov_b32_e32 v24, v181
	v_mul_f32_e32 v26, v33, v26
	v_mul_f32_e32 v30, v25, v30
	v_cvt_pk_fp8_f32 v24, v18, v19
	v_mov_b32_e32 v25, v181
	v_cvt_pk_fp8_f32 v25, v29, v26
	v_add_f32_e32 v18, 1.0, v31
	v_mul_f32_e32 v18, v18, v30
	v_cvt_pk_fp8_f32 v24, v23, v28 op_sel:[0,0,1]
	v_ashrrev_i32_e32 v23, 31, v22
	v_cvt_pk_fp8_f32 v25, v27, v18 op_sel:[0,0,1]
	v_lshlrev_b64 v[18:19], 11, v[22:23]
	v_fmamk_f32 v23, v158, 0x3c800000, v14
	v_min_f32_e32 v23, 0x40e00000, v23
	v_mul_f32_e32 v26, 0xbfd9db23, v23
	v_mul_f32_e32 v26, 0x3fb8aa3b, v26
	v_exp_f32_e32 v26, v26
	v_lshl_add_u64 v[18:19], s[8:9], 0, v[18:19]
	v_lshl_add_u64 v[18:19], v[18:19], 0, v[20:21]
	global_store_dwordx2 v[18:19], v[24:25], off
	v_add_f32_e32 v25, 1.0, v26
	v_fmamk_f32 v26, v159, 0x3c800000, v15
	v_min_f32_e32 v26, 0x40e00000, v26
	v_mul_f32_e32 v27, 0xbfd9db23, v26
	v_mul_f32_e32 v27, 0x3fb8aa3b, v27
	v_rcp_f32_e32 v25, v25
	v_exp_f32_e32 v27, v27
	v_fmamk_f32 v28, v161, 0x3c800000, v17
	v_min_f32_e32 v28, 0x40e00000, v28
	v_mul_f32_e32 v23, v23, v25
	v_add_f32_e32 v25, 1.0, v27
	v_rcp_f32_e32 v25, v25
	v_mul_f32_e32 v29, 0xbfd9db23, v28
	v_mul_f32_e32 v29, 0x3fb8aa3b, v29
	v_exp_f32_e32 v29, v29
	v_mul_f32_e32 v25, v26, v25
	v_fmamk_f32 v26, v160, 0x3c800000, v16
	v_min_f32_e32 v26, 0x40e00000, v26
	v_mul_f32_e32 v27, 0xbfd9db23, v26
	v_mul_f32_e32 v27, 0x3fb8aa3b, v27
	v_exp_f32_e32 v27, v27
	v_fmamk_f32 v30, v151, 0x3c800000, v7
	v_min_f32_e32 v30, 0x40e00000, v30
	v_mul_f32_e32 v31, 0xbfd9db23, v30
	v_add_f32_e32 v27, 1.0, v27
	v_rcp_f32_e32 v27, v27
	v_mul_f32_e32 v31, 0x3fb8aa3b, v31
	v_exp_f32_e32 v31, v31
	v_fmamk_f32 v24, v154, 0x3c800000, v10
	v_mul_f32_e32 v26, v26, v27
	v_add_f32_e32 v27, 1.0, v29
	v_rcp_f32_e32 v27, v27
	v_med3_f32 v24, v24, s57, v196
	v_add_f32_e32 v24, 1.0, v24
	v_mul_f32_e32 v23, v24, v23
	v_mul_f32_e32 v27, v28, v27
	v_fmamk_f32 v28, v150, 0x3c800000, v6
	v_min_f32_e32 v28, 0x40e00000, v28
	v_mul_f32_e32 v29, 0xbfd9db23, v28
	v_mul_f32_e32 v29, 0x3fb8aa3b, v29
	v_exp_f32_e32 v29, v29
	v_fmamk_f32 v24, v155, 0x3c800000, v11
	v_med3_f32 v24, v24, s57, v196
	v_add_f32_e32 v24, 1.0, v24
	v_add_f32_e32 v29, 1.0, v29
	v_rcp_f32_e32 v29, v29
	v_mul_f32_e32 v25, v24, v25
	v_fmamk_f32 v24, v156, 0x3c800000, v12
	v_med3_f32 v24, v24, s57, v196
	v_mul_f32_e32 v28, v28, v29
	v_add_f32_e32 v29, 1.0, v31
	v_rcp_f32_e32 v29, v29
	v_add_f32_e32 v24, 1.0, v24
	v_mul_f32_e32 v26, v24, v26
	v_fmamk_f32 v24, v157, 0x3c800000, v13
	v_mul_f32_e32 v29, v30, v29
	v_fmamk_f32 v30, v152, 0x3c800000, v8
	v_min_f32_e32 v30, 0x40e00000, v30
	v_mul_f32_e32 v31, 0xbfd9db23, v30
	v_med3_f32 v24, v24, s57, v196
	v_mul_f32_e32 v31, 0x3fb8aa3b, v31
	v_add_f32_e32 v24, 1.0, v24
; __device__ __forceinline__ unsigned pk4_fp8(float a, float b, float c, float d) { int p = __builtin_amdgcn_cvt_pk_fp8_f32(a, b, 0, false); p = __builtin_amdgcn_cvt_pk_fp8_f32(c, d, p, true); return (unsigned)p; }
;     __device__ __forceinline__ void operator()(const f32x4 (&acc)[2][2][4][2], const Unit& u, int wr, int wc, int fr, int fq) const {
;     ...
;         for (int ai = 0; ai < 2; ++ai)
; #pragma unroll
;             for (int m = 0; m < 4; ++m) { float r[8];
; #pragma unroll
;                 for (int n = 0; n < 2; ++n)
; #pragma unroll
;                     for (int j = 0; j < 4; ++j) {
;                         float g = acc[ai][0][m][n][j] * W8_INV + bg[n][j], uu = acc[ai][1][m][n][j] * W8_INV + bu[n][j];
;                         g = fminf(g, 7.0f); uu = fminf(fmaxf(uu, -7.0f), 7.0f);
;                         const float glu = g * __builtin_amdgcn_rcpf(1.0f + __expf(-1.702f * g));
;                         r[n * 4 + j] = (uu + 1.0f) * glu; }
;                 u32x2 w; w.x = pk4_fp8(r[0], r[1], r[2], r[3]); w.y = pk4_fp8(r[4], r[5], r[6], r[7]);
;                 *(u32x2*)(O + (size_t)(row0 + ai * HALF + m * 16) * DM + cc) = w; }
	v_exp_f32_e32 v31, v31
	v_mul_f32_e32 v27, v24, v27
	v_fmamk_f32 v24, v146, 0x3c800000, v2
	v_med3_f32 v24, v24, s57, v196
	v_fmamk_f32 v32, v153, 0x3c800000, v9
	v_add_f32_e32 v24, 1.0, v24
	v_min_f32_e32 v32, 0x40e00000, v32
	v_mul_f32_e32 v28, v24, v28
	v_fmamk_f32 v24, v147, 0x3c800000, v3
	v_add_f32_e32 v31, 1.0, v31
	v_mul_f32_e32 v33, 0xbfd9db23, v32
	v_med3_f32 v24, v24, s57, v196
	v_rcp_f32_e32 v31, v31
	v_mul_f32_e32 v33, 0x3fb8aa3b, v33
	v_add_f32_e32 v24, 1.0, v24
	v_exp_f32_e32 v33, v33
	v_mul_f32_e32 v29, v24, v29
	v_fmamk_f32 v24, v148, 0x3c800000, v4
	v_med3_f32 v24, v24, s57, v196
	v_mul_f32_e32 v30, v30, v31
	v_add_f32_e32 v24, 1.0, v24
	v_add_f32_e32 v31, 1.0, v33
	v_mul_f32_e32 v30, v24, v30
	v_fmamk_f32 v24, v149, 0x3c800000, v5
	v_rcp_f32_e32 v31, v31
	v_med3_f32 v33, v24, s57, v196
	v_mov_b32_e32 v24, v181
	v_cvt_pk_fp8_f32 v24, v23, v25
	v_mov_b32_e32 v25, v181
	v_cvt_pk_fp8_f32 v25, v28, v29
	v_mul_f32_e32 v31, v32, v31
	v_add_f32_e32 v23, 1.0, v33
	v_mul_f32_e32 v23, v23, v31
	v_cvt_pk_fp8_f32 v24, v26, v27 op_sel:[0,0,1]
	v_cvt_pk_fp8_f32 v25, v30, v23 op_sel:[0,0,1]
	v_or_b32_e32 v26, 16, v22
	v_fmamk_f32 v23, v142, 0x3c800000, v14
	v_ashrrev_i32_e32 v27, 31, v26
	v_min_f32_e32 v23, 0x40e00000, v23
	v_lshlrev_b64 v[26:27], 11, v[26:27]
	v_mul_f32_e32 v28, 0xbfd9db23, v23
	v_lshl_add_u64 v[26:27], s[8:9], 0, v[26:27]
	v_mul_f32_e32 v28, 0x3fb8aa3b, v28
	v_exp_f32_e32 v28, v28
	v_lshl_add_u64 v[26:27], v[26:27], 0, v[20:21]
	global_store_dwordx2 v[26:27], v[24:25], off
	v_fmamk_f32 v26, v143, 0x3c800000, v15
	v_min_f32_e32 v26, 0x40e00000, v26
	v_mul_f32_e32 v27, 0xbfd9db23, v26
	v_add_f32_e32 v25, 1.0, v28
	v_mul_f32_e32 v27, 0x3fb8aa3b, v27
	v_rcp_f32_e32 v25, v25
	v_exp_f32_e32 v27, v27
	v_fmamk_f32 v28, v145, 0x3c800000, v17
	v_min_f32_e32 v28, 0x40e00000, v28
	v_mul_f32_e32 v23, v23, v25
	v_add_f32_e32 v25, 1.0, v27
	v_rcp_f32_e32 v25, v25
	v_mul_f32_e32 v29, 0xbfd9db23, v28
	v_mul_f32_e32 v29, 0x3fb8aa3b, v29
	v_exp_f32_e32 v29, v29
	v_mul_f32_e32 v25, v26, v25
	v_fmamk_f32 v26, v144, 0x3c800000, v16
	v_min_f32_e32 v26, 0x40e00000, v26
	v_mul_f32_e32 v27, 0xbfd9db23, v26
	v_mul_f32_e32 v27, 0x3fb8aa3b, v27
	v_exp_f32_e32 v27, v27
	v_fmamk_f32 v30, v135, 0x3c800000, v7
	v_min_f32_e32 v30, 0x40e00000, v30
	v_mul_f32_e32 v31, 0xbfd9db23, v30
	v_add_f32_e32 v27, 1.0, v27
	v_rcp_f32_e32 v27, v27
	v_mul_f32_e32 v31, 0x3fb8aa3b, v31
	v_exp_f32_e32 v31, v31
	v_fmamk_f32 v24, v138, 0x3c800000, v10
	v_mul_f32_e32 v26, v26, v27
	v_add_f32_e32 v27, 1.0, v29
	v_rcp_f32_e32 v27, v27
	v_med3_f32 v24, v24, s57, v196
	v_add_f32_e32 v24, 1.0, v24
	v_mul_f32_e32 v23, v24, v23
	v_mul_f32_e32 v27, v28, v27
	v_fmamk_f32 v28, v134, 0x3c800000, v6
	v_min_f32_e32 v28, 0x40e00000, v28
	v_mul_f32_e32 v29, 0xbfd9db23, v28
	v_mul_f32_e32 v29, 0x3fb8aa3b, v29
	v_exp_f32_e32 v29, v29
	v_fmamk_f32 v24, v139, 0x3c800000, v11
	v_med3_f32 v24, v24, s57, v196
	v_add_f32_e32 v24, 1.0, v24
	v_add_f32_e32 v29, 1.0, v29
	v_rcp_f32_e32 v29, v29
	v_mul_f32_e32 v25, v24, v25
	v_fmamk_f32 v24, v140, 0x3c800000, v12
	v_med3_f32 v24, v24, s57, v196
	v_mul_f32_e32 v28, v28, v29
	v_add_f32_e32 v29, 1.0, v31
	v_rcp_f32_e32 v29, v29
	v_add_f32_e32 v24, 1.0, v24
	v_mul_f32_e32 v26, v24, v26
	v_fmamk_f32 v24, v141, 0x3c800000, v13
	v_mul_f32_e32 v29, v30, v29
	v_fmamk_f32 v30, v136, 0x3c800000, v8
	v_min_f32_e32 v30, 0x40e00000, v30
	v_mul_f32_e32 v31, 0xbfd9db23, v30
	v_med3_f32 v24, v24, s57, v196
	v_mul_f32_e32 v31, 0x3fb8aa3b, v31
	v_add_f32_e32 v24, 1.0, v24
	v_exp_f32_e32 v31, v31
	v_mul_f32_e32 v27, v24, v27
	v_fmamk_f32 v24, v130, 0x3c800000, v2
	v_med3_f32 v24, v24, s57, v196
	v_fmamk_f32 v32, v137, 0x3c800000, v9
	v_add_f32_e32 v24, 1.0, v24
	v_min_f32_e32 v32, 0x40e00000, v32
	v_mul_f32_e32 v28, v24, v28
	v_fmamk_f32 v24, v131, 0x3c800000, v3
	v_add_f32_e32 v31, 1.0, v31
	v_mul_f32_e32 v33, 0xbfd9db23, v32
	v_med3_f32 v24, v24, s57, v196
	v_rcp_f32_e32 v31, v31
	v_mul_f32_e32 v33, 0x3fb8aa3b, v33
	v_add_f32_e32 v24, 1.0, v24
	v_exp_f32_e32 v33, v33
	v_mul_f32_e32 v29, v24, v29
	v_fmamk_f32 v24, v132, 0x3c800000, v4
	v_med3_f32 v24, v24, s57, v196
	v_mul_f32_e32 v30, v30, v31
	v_add_f32_e32 v24, 1.0, v24
	v_add_f32_e32 v31, 1.0, v33
	v_mul_f32_e32 v30, v24, v30
	v_fmamk_f32 v24, v133, 0x3c800000, v5
	v_rcp_f32_e32 v31, v31
	v_med3_f32 v33, v24, s57, v196
	v_mov_b32_e32 v24, v181
	v_cvt_pk_fp8_f32 v24, v23, v25
	v_mov_b32_e32 v25, v181
	v_cvt_pk_fp8_f32 v25, v28, v29
	v_mul_f32_e32 v31, v32, v31
	v_add_f32_e32 v23, 1.0, v33
	v_mul_f32_e32 v23, v23, v31
	v_cvt_pk_fp8_f32 v24, v26, v27 op_sel:[0,0,1]
	v_cvt_pk_fp8_f32 v25, v30, v23 op_sel:[0,0,1]
	v_or_b32_e32 v26, 32, v22
	v_fmamk_f32 v23, v126, 0x3c800000, v14
	v_ashrrev_i32_e32 v27, 31, v26
	v_min_f32_e32 v23, 0x40e00000, v23
	v_lshlrev_b64 v[26:27], 11, v[26:27]
	v_mul_f32_e32 v28, 0xbfd9db23, v23
	v_lshl_add_u64 v[26:27], s[8:9], 0, v[26:27]
	v_mul_f32_e32 v28, 0x3fb8aa3b, v28
	v_exp_f32_e32 v28, v28
	v_lshl_add_u64 v[26:27], v[26:27], 0, v[20:21]
	global_store_dwordx2 v[26:27], v[24:25], off
	v_fmamk_f32 v26, v127, 0x3c800000, v15
	v_min_f32_e32 v26, 0x40e00000, v26
	v_mul_f32_e32 v27, 0xbfd9db23, v26
	v_add_f32_e32 v25, 1.0, v28
	v_mul_f32_e32 v27, 0x3fb8aa3b, v27
	v_rcp_f32_e32 v25, v25
	v_exp_f32_e32 v27, v27
	v_fmamk_f32 v28, v129, 0x3c800000, v17
	v_min_f32_e32 v28, 0x40e00000, v28
	v_mul_f32_e32 v23, v23, v25
	v_add_f32_e32 v25, 1.0, v27
	v_rcp_f32_e32 v25, v25
	v_mul_f32_e32 v29, 0xbfd9db23, v28
	v_mul_f32_e32 v29, 0x3fb8aa3b, v29
	v_exp_f32_e32 v29, v29
	v_mul_f32_e32 v25, v26, v25
	v_fmamk_f32 v26, v128, 0x3c800000, v16
	v_min_f32_e32 v26, 0x40e00000, v26
	v_mul_f32_e32 v27, 0xbfd9db23, v26
; __device__ __forceinline__ unsigned pk4_fp8(float a, float b, float c, float d) { int p = __builtin_amdgcn_cvt_pk_fp8_f32(a, b, 0, false); p = __builtin_amdgcn_cvt_pk_fp8_f32(c, d, p, true); return (unsigned)p; }
;     __device__ __forceinline__ void operator()(const f32x4 (&acc)[2][2][4][2], const Unit& u, int wr, int wc, int fr, int fq) const {
;     ...
;         for (int ai = 0; ai < 2; ++ai)
; #pragma unroll
;             for (int m = 0; m < 4; ++m) { float r[8];
; #pragma unroll
;                 for (int n = 0; n < 2; ++n)
; #pragma unroll
;                     for (int j = 0; j < 4; ++j) {
;                         float g = acc[ai][0][m][n][j] * W8_INV + bg[n][j], uu = acc[ai][1][m][n][j] * W8_INV + bu[n][j];
;                         g = fminf(g, 7.0f); uu = fminf(fmaxf(uu, -7.0f), 7.0f);
;                         const float glu = g * __builtin_amdgcn_rcpf(1.0f + __expf(-1.702f * g));
;                         r[n * 4 + j] = (uu + 1.0f) * glu; }
;                 u32x2 w; w.x = pk4_fp8(r[0], r[1], r[2], r[3]); w.y = pk4_fp8(r[4], r[5], r[6], r[7]);
;                 *(u32x2*)(O + (size_t)(row0 + ai * HALF + m * 16) * DM + cc) = w; }
	v_mul_f32_e32 v27, 0x3fb8aa3b, v27
	v_exp_f32_e32 v27, v27
	v_fmamk_f32 v30, v119, 0x3c800000, v7
	v_min_f32_e32 v30, 0x40e00000, v30
	v_mul_f32_e32 v31, 0xbfd9db23, v30
	v_add_f32_e32 v27, 1.0, v27
	v_rcp_f32_e32 v27, v27
	v_mul_f32_e32 v31, 0x3fb8aa3b, v31
	v_exp_f32_e32 v31, v31
	v_fmamk_f32 v24, v122, 0x3c800000, v10
	v_mul_f32_e32 v26, v26, v27
	v_add_f32_e32 v27, 1.0, v29
	v_rcp_f32_e32 v27, v27
	v_med3_f32 v24, v24, s57, v196
	v_add_f32_e32 v24, 1.0, v24
	v_mul_f32_e32 v23, v24, v23
	v_mul_f32_e32 v27, v28, v27
	v_fmamk_f32 v28, v118, 0x3c800000, v6
	v_min_f32_e32 v28, 0x40e00000, v28
	v_mul_f32_e32 v29, 0xbfd9db23, v28
	v_mul_f32_e32 v29, 0x3fb8aa3b, v29
	v_exp_f32_e32 v29, v29
	v_fmamk_f32 v24, v123, 0x3c800000, v11
	v_med3_f32 v24, v24, s57, v196
	v_add_f32_e32 v24, 1.0, v24
	v_add_f32_e32 v29, 1.0, v29
	v_rcp_f32_e32 v29, v29
	v_mul_f32_e32 v25, v24, v25
	v_fmamk_f32 v24, v124, 0x3c800000, v12
	v_med3_f32 v24, v24, s57, v196
	v_mul_f32_e32 v28, v28, v29
	v_add_f32_e32 v29, 1.0, v31
	v_rcp_f32_e32 v29, v29
	v_add_f32_e32 v24, 1.0, v24
	v_mul_f32_e32 v26, v24, v26
	v_fmamk_f32 v24, v125, 0x3c800000, v13
	v_mul_f32_e32 v29, v30, v29
	v_fmamk_f32 v30, v120, 0x3c800000, v8
	v_min_f32_e32 v30, 0x40e00000, v30
	v_mul_f32_e32 v31, 0xbfd9db23, v30
	v_med3_f32 v24, v24, s57, v196
	v_mul_f32_e32 v31, 0x3fb8aa3b, v31
	v_add_f32_e32 v24, 1.0, v24
	v_exp_f32_e32 v31, v31
	v_mul_f32_e32 v27, v24, v27
	v_fmamk_f32 v24, v114, 0x3c800000, v2
	v_med3_f32 v24, v24, s57, v196
	v_fmamk_f32 v32, v121, 0x3c800000, v9
	v_add_f32_e32 v24, 1.0, v24
	v_min_f32_e32 v32, 0x40e00000, v32
	v_mul_f32_e32 v28, v24, v28
	v_fmamk_f32 v24, v115, 0x3c800000, v3
	v_add_f32_e32 v31, 1.0, v31
	v_mul_f32_e32 v33, 0xbfd9db23, v32
	v_med3_f32 v24, v24, s57, v196
	v_rcp_f32_e32 v31, v31
	v_mul_f32_e32 v33, 0x3fb8aa3b, v33
	v_add_f32_e32 v24, 1.0, v24
	v_exp_f32_e32 v33, v33
	v_mul_f32_e32 v29, v24, v29
	v_fmamk_f32 v24, v116, 0x3c800000, v4
	v_med3_f32 v24, v24, s57, v196
	v_mul_f32_e32 v30, v30, v31
	v_add_f32_e32 v24, 1.0, v24
	v_add_f32_e32 v31, 1.0, v33
	v_mul_f32_e32 v30, v24, v30
	v_fmamk_f32 v24, v117, 0x3c800000, v5
	v_rcp_f32_e32 v31, v31
	v_med3_f32 v33, v24, s57, v196
	v_mov_b32_e32 v24, v181
	v_cvt_pk_fp8_f32 v24, v23, v25
	v_mov_b32_e32 v25, v181
	v_cvt_pk_fp8_f32 v25, v28, v29
	v_mul_f32_e32 v31, v32, v31
	v_add_f32_e32 v23, 1.0, v33
	v_mul_f32_e32 v23, v23, v31
	v_or_b32_e32 v22, 48, v22
	v_cvt_pk_fp8_f32 v25, v30, v23 op_sel:[0,0,1]
	v_ashrrev_i32_e32 v23, 31, v22
	v_lshlrev_b64 v[22:23], 11, v[22:23]
	v_lshl_add_u64 v[22:23], s[8:9], 0, v[22:23]
	v_lshl_add_u64 v[20:21], v[22:23], 0, v[20:21]
	v_fmamk_f32 v22, v111, 0x3c800000, v15
	v_min_f32_e32 v22, 0x40e00000, v22
	v_mul_f32_e32 v23, 0xbfd9db23, v22
	v_mul_f32_e32 v23, 0x3fb8aa3b, v23
	v_exp_f32_e32 v23, v23
	v_cvt_pk_fp8_f32 v24, v26, v27 op_sel:[0,0,1]
	v_fmamk_f32 v26, v110, 0x3c800000, v14
	v_min_f32_e32 v26, 0x40e00000, v26
	v_add_f32_e32 v23, 1.0, v23
	v_mul_f32_e32 v27, 0xbfd9db23, v26
	v_rcp_f32_e32 v23, v23
	v_mul_f32_e32 v27, 0x3fb8aa3b, v27
	v_exp_f32_e32 v27, v27
	global_store_dwordx2 v[20:21], v[24:25], off
	v_mul_f32_e32 v22, v22, v23
	v_fmamk_f32 v23, v112, 0x3c800000, v16
	v_min_f32_e32 v23, 0x40e00000, v23
	v_add_f32_e32 v21, 1.0, v27
	v_mul_f32_e32 v24, 0xbfd9db23, v23
	v_rcp_f32_e32 v21, v21
	v_mul_f32_e32 v24, 0x3fb8aa3b, v24
	v_exp_f32_e32 v24, v24
	v_fmamk_f32 v25, v113, 0x3c800000, v17
	v_min_f32_e32 v25, 0x40e00000, v25
	v_mul_f32_e32 v21, v26, v21
	v_mul_f32_e32 v26, 0xbfd9db23, v25
	v_add_f32_e32 v24, 1.0, v24
	v_mul_f32_e32 v26, 0x3fb8aa3b, v26
	v_rcp_f32_e32 v24, v24
	v_exp_f32_e32 v26, v26
	v_fmamk_f32 v27, v103, 0x3c800000, v7
	v_min_f32_e32 v27, 0x40e00000, v27
	v_mul_f32_e32 v23, v23, v24
	v_add_f32_e32 v24, 1.0, v26
	v_rcp_f32_e32 v24, v24
	v_mul_f32_e32 v28, 0xbfd9db23, v27
	v_mul_f32_e32 v28, 0x3fb8aa3b, v28
	v_exp_f32_e32 v28, v28
	v_mul_f32_e32 v24, v25, v24
	v_fmamk_f32 v25, v102, 0x3c800000, v6
	v_min_f32_e32 v25, 0x40e00000, v25
	v_mul_f32_e32 v26, 0xbfd9db23, v25
	v_mul_f32_e32 v26, 0x3fb8aa3b, v26
	v_exp_f32_e32 v26, v26
	v_fmamk_f32 v20, v106, 0x3c800000, v10
	v_med3_f32 v20, v20, s57, v196
	v_add_f32_e32 v20, 1.0, v20
	v_add_f32_e32 v26, 1.0, v26
	v_rcp_f32_e32 v26, v26
	v_mul_f32_e32 v21, v20, v21
	v_fmamk_f32 v20, v107, 0x3c800000, v11
	v_med3_f32 v20, v20, s57, v196
	v_mul_f32_e32 v25, v25, v26
	v_add_f32_e32 v26, 1.0, v28
	v_rcp_f32_e32 v26, v26
	v_add_f32_e32 v20, 1.0, v20
	v_mul_f32_e32 v22, v20, v22
	v_fmamk_f32 v20, v108, 0x3c800000, v12
	v_med3_f32 v20, v20, s57, v196
	v_mul_f32_e32 v26, v27, v26
	v_fmamk_f32 v27, v104, 0x3c800000, v8
	v_add_f32_e32 v20, 1.0, v20
	v_min_f32_e32 v27, 0x40e00000, v27
	v_mul_f32_e32 v23, v20, v23
	v_fmamk_f32 v20, v109, 0x3c800000, v13
	v_mul_f32_e32 v28, 0xbfd9db23, v27
	v_med3_f32 v20, v20, s57, v196
	v_mul_f32_e32 v28, 0x3fb8aa3b, v28
	v_add_f32_e32 v20, 1.0, v20
	v_exp_f32_e32 v28, v28
	v_mul_f32_e32 v24, v20, v24
	v_fmamk_f32 v20, v98, 0x3c800000, v2
	v_med3_f32 v20, v20, s57, v196
	v_fmamk_f32 v29, v105, 0x3c800000, v9
	v_add_f32_e32 v20, 1.0, v20
	v_min_f32_e32 v29, 0x40e00000, v29
	v_mul_f32_e32 v25, v20, v25
	v_fmamk_f32 v20, v99, 0x3c800000, v3
	v_add_f32_e32 v28, 1.0, v28
	v_mul_f32_e32 v30, 0xbfd9db23, v29
	v_med3_f32 v20, v20, s57, v196
	v_rcp_f32_e32 v28, v28
	v_mul_f32_e32 v30, 0x3fb8aa3b, v30
	v_add_f32_e32 v20, 1.0, v20
	v_exp_f32_e32 v30, v30
	v_mul_f32_e32 v26, v20, v26
	v_fmamk_f32 v20, v100, 0x3c800000, v4
	v_med3_f32 v20, v20, s57, v196
	v_mul_f32_e32 v27, v27, v28
	v_add_f32_e32 v20, 1.0, v20
	v_add_f32_e32 v28, 1.0, v30
	v_mul_f32_e32 v27, v20, v27
	v_fmamk_f32 v20, v101, 0x3c800000, v5
; __device__ __forceinline__ unsigned pk4_fp8(float a, float b, float c, float d) { int p = __builtin_amdgcn_cvt_pk_fp8_f32(a, b, 0, false); p = __builtin_amdgcn_cvt_pk_fp8_f32(c, d, p, true); return (unsigned)p; }
;     __device__ __forceinline__ void operator()(const f32x4 (&acc)[2][2][4][2], const Unit& u, int wr, int wc, int fr, int fq) const {
;     ...
;         for (int ai = 0; ai < 2; ++ai)
; #pragma unroll
;             for (int m = 0; m < 4; ++m) { float r[8];
; #pragma unroll
;                 for (int n = 0; n < 2; ++n)
; #pragma unroll
;                     for (int j = 0; j < 4; ++j) {
;                         float g = acc[ai][0][m][n][j] * W8_INV + bg[n][j], uu = acc[ai][1][m][n][j] * W8_INV + bu[n][j];
;                         g = fminf(g, 7.0f); uu = fminf(fmaxf(uu, -7.0f), 7.0f);
;                         const float glu = g * __builtin_amdgcn_rcpf(1.0f + __expf(-1.702f * g));
;                         r[n * 4 + j] = (uu + 1.0f) * glu; }
;                 u32x2 w; w.x = pk4_fp8(r[0], r[1], r[2], r[3]); w.y = pk4_fp8(r[4], r[5], r[6], r[7]);
;                 *(u32x2*)(O + (size_t)(row0 + ai * HALF + m * 16) * DM + cc) = w; }
	v_rcp_f32_e32 v28, v28
	v_med3_f32 v30, v20, s57, v196
	v_mov_b32_e32 v20, v181
	v_cvt_pk_fp8_f32 v20, v21, v22
	v_mov_b32_e32 v21, v181
	v_cvt_pk_fp8_f32 v21, v25, v26
	v_mul_f32_e32 v28, v29, v28
	v_add_f32_e32 v22, 1.0, v30
	v_mul_f32_e32 v22, v22, v28
	v_cvt_pk_fp8_f32 v21, v27, v22 op_sel:[0,0,1]
	v_fmamk_f32 v22, v94, 0x3c800000, v14
	v_cvt_pk_fp8_f32 v20, v23, v24 op_sel:[0,0,1]
	v_min_f32_e32 v24, 0x40e00000, v22
	v_mul_f32_e32 v22, 0xbfd9db23, v24
	v_mul_f32_e32 v22, 0x3fb8aa3b, v22
	v_exp_f32_e32 v25, v22
	v_add_co_u32_e32 v22, vcc, s58, v18
	v_fmamk_f32 v27, v87, 0x3c800000, v7
	s_nop 0
	v_addc_co_u32_e32 v23, vcc, 0, v19, vcc
	global_store_dwordx2 v[22:23], v[20:21], off
	v_fmamk_f32 v22, v95, 0x3c800000, v15
	v_min_f32_e32 v22, 0x40e00000, v22
	v_mul_f32_e32 v23, 0xbfd9db23, v22
	v_mul_f32_e32 v23, 0x3fb8aa3b, v23
	v_exp_f32_e32 v23, v23
	v_add_f32_e32 v21, 1.0, v25
	v_rcp_f32_e32 v21, v21
	v_fmamk_f32 v25, v97, 0x3c800000, v17
	v_add_f32_e32 v23, 1.0, v23
	v_rcp_f32_e32 v23, v23
	v_mul_f32_e32 v21, v24, v21
	v_min_f32_e32 v25, 0x40e00000, v25
	v_mul_f32_e32 v26, 0xbfd9db23, v25
	v_mul_f32_e32 v22, v22, v23
	v_fmamk_f32 v23, v96, 0x3c800000, v16
	v_min_f32_e32 v23, 0x40e00000, v23
	v_mul_f32_e32 v24, 0xbfd9db23, v23
	v_mul_f32_e32 v24, 0x3fb8aa3b, v24
	v_exp_f32_e32 v24, v24
	v_mul_f32_e32 v26, 0x3fb8aa3b, v26
	v_exp_f32_e32 v26, v26
	v_min_f32_e32 v27, 0x40e00000, v27
	v_add_f32_e32 v24, 1.0, v24
	v_rcp_f32_e32 v24, v24
	v_mul_f32_e32 v28, 0xbfd9db23, v27
	v_mul_f32_e32 v28, 0x3fb8aa3b, v28
	v_exp_f32_e32 v28, v28
	v_mul_f32_e32 v23, v23, v24
	v_add_f32_e32 v24, 1.0, v26
	v_rcp_f32_e32 v24, v24
	v_fmamk_f32 v20, v90, 0x3c800000, v10
	v_med3_f32 v20, v20, s57, v196
	v_add_f32_e32 v20, 1.0, v20
	v_mul_f32_e32 v24, v25, v24
	v_fmamk_f32 v25, v86, 0x3c800000, v6
	v_min_f32_e32 v25, 0x40e00000, v25
	v_mul_f32_e32 v26, 0xbfd9db23, v25
	v_mul_f32_e32 v26, 0x3fb8aa3b, v26
	v_exp_f32_e32 v26, v26
	v_mul_f32_e32 v21, v20, v21
	v_fmamk_f32 v20, v91, 0x3c800000, v11
	v_med3_f32 v20, v20, s57, v196
	v_add_f32_e32 v26, 1.0, v26
	v_rcp_f32_e32 v26, v26
	v_add_f32_e32 v20, 1.0, v20
	v_mul_f32_e32 v22, v20, v22
	v_fmamk_f32 v20, v92, 0x3c800000, v12
	v_mul_f32_e32 v25, v25, v26
	v_add_f32_e32 v26, 1.0, v28
	v_rcp_f32_e32 v26, v26
	v_med3_f32 v20, v20, s57, v196
	v_add_f32_e32 v20, 1.0, v20
	v_mul_f32_e32 v23, v20, v23
	v_mul_f32_e32 v26, v27, v26
	v_fmamk_f32 v27, v88, 0x3c800000, v8
	v_min_f32_e32 v27, 0x40e00000, v27
	v_fmamk_f32 v20, v93, 0x3c800000, v13
	v_mul_f32_e32 v28, 0xbfd9db23, v27
	v_med3_f32 v20, v20, s57, v196
	v_mul_f32_e32 v28, 0x3fb8aa3b, v28
	v_add_f32_e32 v20, 1.0, v20
	v_exp_f32_e32 v28, v28
	v_mul_f32_e32 v24, v20, v24
	v_fmamk_f32 v20, v82, 0x3c800000, v2
	v_med3_f32 v20, v20, s57, v196
	v_fmamk_f32 v29, v89, 0x3c800000, v9
	v_add_f32_e32 v20, 1.0, v20
	v_min_f32_e32 v29, 0x40e00000, v29
	v_mul_f32_e32 v25, v20, v25
	v_fmamk_f32 v20, v83, 0x3c800000, v3
	v_add_f32_e32 v28, 1.0, v28
	v_mul_f32_e32 v30, 0xbfd9db23, v29
	v_med3_f32 v20, v20, s57, v196
	v_rcp_f32_e32 v28, v28
	v_mul_f32_e32 v30, 0x3fb8aa3b, v30
	v_add_f32_e32 v20, 1.0, v20
	v_exp_f32_e32 v30, v30
	v_mul_f32_e32 v26, v20, v26
	v_fmamk_f32 v20, v84, 0x3c800000, v4
	v_med3_f32 v20, v20, s57, v196
	v_mul_f32_e32 v27, v27, v28
	v_add_f32_e32 v20, 1.0, v20
	v_add_f32_e32 v28, 1.0, v30
	v_mul_f32_e32 v27, v20, v27
	v_fmamk_f32 v20, v85, 0x3c800000, v5
	v_rcp_f32_e32 v28, v28
	v_med3_f32 v30, v20, s57, v196
	v_mov_b32_e32 v20, v181
	v_cvt_pk_fp8_f32 v20, v21, v22
	v_mov_b32_e32 v21, v181
	v_cvt_pk_fp8_f32 v21, v25, v26
	v_mul_f32_e32 v28, v29, v28
	v_add_f32_e32 v22, 1.0, v30
	v_mul_f32_e32 v22, v22, v28
	v_cvt_pk_fp8_f32 v21, v27, v22 op_sel:[0,0,1]
	v_fmamk_f32 v22, v78, 0x3c800000, v14
	v_cvt_pk_fp8_f32 v20, v23, v24 op_sel:[0,0,1]
	v_min_f32_e32 v24, 0x40e00000, v22
	v_mul_f32_e32 v22, 0xbfd9db23, v24
	v_mul_f32_e32 v22, 0x3fb8aa3b, v22
	v_exp_f32_e32 v25, v22
	v_add_co_u32_e32 v22, vcc, s59, v18
	v_fmamk_f32 v27, v71, 0x3c800000, v7
	s_nop 0
	v_addc_co_u32_e32 v23, vcc, 0, v19, vcc
	global_store_dwordx2 v[22:23], v[20:21], off
	v_fmamk_f32 v22, v79, 0x3c800000, v15
	v_min_f32_e32 v22, 0x40e00000, v22
	v_mul_f32_e32 v23, 0xbfd9db23, v22
	v_mul_f32_e32 v23, 0x3fb8aa3b, v23
	v_exp_f32_e32 v23, v23
	v_add_f32_e32 v21, 1.0, v25
	v_rcp_f32_e32 v21, v21
	v_fmamk_f32 v25, v81, 0x3c800000, v17
	v_add_f32_e32 v23, 1.0, v23
	v_rcp_f32_e32 v23, v23
	v_mul_f32_e32 v21, v24, v21
	v_min_f32_e32 v25, 0x40e00000, v25
	v_mul_f32_e32 v26, 0xbfd9db23, v25
	v_mul_f32_e32 v22, v22, v23
	v_fmamk_f32 v23, v80, 0x3c800000, v16
	v_min_f32_e32 v23, 0x40e00000, v23
	v_mul_f32_e32 v24, 0xbfd9db23, v23
	v_mul_f32_e32 v24, 0x3fb8aa3b, v24
	v_exp_f32_e32 v24, v24
	v_mul_f32_e32 v26, 0x3fb8aa3b, v26
	v_exp_f32_e32 v26, v26
	v_min_f32_e32 v27, 0x40e00000, v27
	v_add_f32_e32 v24, 1.0, v24
	v_rcp_f32_e32 v24, v24
	v_mul_f32_e32 v28, 0xbfd9db23, v27
	v_mul_f32_e32 v28, 0x3fb8aa3b, v28
	v_exp_f32_e32 v28, v28
	v_mul_f32_e32 v23, v23, v24
	v_add_f32_e32 v24, 1.0, v26
	v_rcp_f32_e32 v24, v24
	v_fmamk_f32 v20, v74, 0x3c800000, v10
	v_med3_f32 v20, v20, s57, v196
	v_add_f32_e32 v20, 1.0, v20
	v_mul_f32_e32 v24, v25, v24
	v_fmamk_f32 v25, v70, 0x3c800000, v6
	v_min_f32_e32 v25, 0x40e00000, v25
; __device__ __forceinline__ unsigned pk4_fp8(float a, float b, float c, float d) { int p = __builtin_amdgcn_cvt_pk_fp8_f32(a, b, 0, false); p = __builtin_amdgcn_cvt_pk_fp8_f32(c, d, p, true); return (unsigned)p; }
; __device__ __forceinline__ unsigned pk4_fp8_scaled(float a, float b, float c, float d) { s16x2 r = {0, 0}; r = __builtin_amdgcn_cvt_scalef32_pk_fp8_f32(r, a, b, pg8::W8_INV, false); r = __builtin_amdgcn_cvt_scalef32_pk_fp8_f32(r, c, d, pg8::W8_INV, true); return __builtin_bit_cast(unsigned, r); }
;     __device__ __forceinline__ void operator()(const f32x4 (&acc)[2][2][4][2], const Unit& u, int wr, int wc, int fr, int fq) const {
;     ...
;         for (int ai = 0; ai < 2; ++ai)
; #pragma unroll
;             for (int m = 0; m < 4; ++m) { float r[8];
; #pragma unroll
;                 for (int n = 0; n < 2; ++n)
; #pragma unroll
;                     for (int j = 0; j < 4; ++j) {
;                         float g = acc[ai][0][m][n][j] * W8_INV + bg[n][j], uu = acc[ai][1][m][n][j] * W8_INV + bu[n][j];
;                         g = fminf(g, 7.0f); uu = fminf(fmaxf(uu, -7.0f), 7.0f);
;                         const float glu = g * __builtin_amdgcn_rcpf(1.0f + __expf(-1.702f * g));
;                         r[n * 4 + j] = (uu + 1.0f) * glu; }
;                 u32x2 w; w.x = pk4_fp8(r[0], r[1], r[2], r[3]); w.y = pk4_fp8(r[4], r[5], r[6], r[7]);
;                 *(u32x2*)(O + (size_t)(row0 + ai * HALF + m * 16) * DM + cc) = w; }
; __device__ __forceinline__ void sjob_load(const SJob& c, f32x4 (&v)[8]) {
; #pragma unroll
;     for (int r = 0; r < 8; ++r) v[r] = __builtin_nontemporal_load((const f32x4*)(c.src + (size_t)r * c.ld));
; }
; __device__ __forceinline__ void sjob_store(const SJob& c, const f32x4 (&v)[8]) {
; #pragma unroll
;     for (int jn = 0; jn < 4; ++jn) { u32x2 o;
;         o.x = pk4_fp8_scaled(v[0][jn], v[1][jn], v[2][jn], v[3][jn]); o.y = pk4_fp8_scaled(v[4][jn], v[5][jn], v[6][jn], v[7][jn]);
;         __builtin_nontemporal_store(o, (u32x2*)(c.dst + (size_t)jn * 2048)); }
; }
	v_mul_f32_e32 v26, 0xbfd9db23, v25
	v_mul_f32_e32 v26, 0x3fb8aa3b, v26
	v_exp_f32_e32 v26, v26
	v_mul_f32_e32 v21, v20, v21
	v_fmamk_f32 v20, v75, 0x3c800000, v11
	v_med3_f32 v20, v20, s57, v196
	v_add_f32_e32 v26, 1.0, v26
	v_rcp_f32_e32 v26, v26
	v_add_f32_e32 v20, 1.0, v20
	v_mul_f32_e32 v22, v20, v22
	v_fmamk_f32 v20, v76, 0x3c800000, v12
	v_mul_f32_e32 v25, v25, v26
	v_add_f32_e32 v26, 1.0, v28
	v_rcp_f32_e32 v26, v26
	v_med3_f32 v20, v20, s57, v196
	v_add_f32_e32 v20, 1.0, v20
	v_mul_f32_e32 v23, v20, v23
	v_mul_f32_e32 v26, v27, v26
	v_fmamk_f32 v27, v72, 0x3c800000, v8
	v_min_f32_e32 v27, 0x40e00000, v27
	v_fmamk_f32 v20, v77, 0x3c800000, v13
	v_mul_f32_e32 v28, 0xbfd9db23, v27
	v_med3_f32 v20, v20, s57, v196
	v_mul_f32_e32 v28, 0x3fb8aa3b, v28
	v_add_f32_e32 v20, 1.0, v20
	v_exp_f32_e32 v28, v28
	v_mul_f32_e32 v24, v20, v24
	v_fmamk_f32 v20, v66, 0x3c800000, v2
	v_med3_f32 v20, v20, s57, v196
	v_fmamk_f32 v29, v73, 0x3c800000, v9
	v_add_f32_e32 v20, 1.0, v20
	v_min_f32_e32 v29, 0x40e00000, v29
	v_mul_f32_e32 v25, v20, v25
	v_fmamk_f32 v20, v67, 0x3c800000, v3
	v_add_f32_e32 v28, 1.0, v28
	v_mul_f32_e32 v30, 0xbfd9db23, v29
	v_med3_f32 v20, v20, s57, v196
	v_rcp_f32_e32 v28, v28
	v_mul_f32_e32 v30, 0x3fb8aa3b, v30
	v_add_f32_e32 v20, 1.0, v20
	v_exp_f32_e32 v30, v30
	v_mul_f32_e32 v26, v20, v26
	v_fmamk_f32 v20, v68, 0x3c800000, v4
	v_med3_f32 v20, v20, s57, v196
	v_mul_f32_e32 v27, v27, v28
	v_add_f32_e32 v20, 1.0, v20
	v_add_f32_e32 v28, 1.0, v30
	v_mul_f32_e32 v27, v20, v27
	v_fmamk_f32 v20, v69, 0x3c800000, v5
	v_rcp_f32_e32 v28, v28
	v_med3_f32 v30, v20, s57, v196
	v_mov_b32_e32 v20, v181
	v_cvt_pk_fp8_f32 v20, v21, v22
	v_mov_b32_e32 v21, v181
	v_cvt_pk_fp8_f32 v21, v25, v26
	v_mul_f32_e32 v28, v29, v28
	v_add_f32_e32 v22, 1.0, v30
	v_fmamk_f32 v14, v62, 0x3c800000, v14
	v_mul_f32_e32 v22, v22, v28
	v_min_f32_e32 v14, 0x40e00000, v14
	v_cvt_pk_fp8_f32 v21, v27, v22 op_sel:[0,0,1]
	v_mul_f32_e32 v22, 0xbfd9db23, v14
	v_cvt_pk_fp8_f32 v20, v23, v24 op_sel:[0,0,1]
	v_mul_f32_e32 v22, 0x3fb8aa3b, v22
	v_exp_f32_e32 v24, v22
	v_add_co_u32_e32 v22, vcc, s60, v18
	v_fmamk_f32 v15, v63, 0x3c800000, v15
	s_nop 0
	v_addc_co_u32_e32 v23, vcc, 0, v19, vcc
	v_min_f32_e32 v15, 0x40e00000, v15
	global_store_dwordx2 v[22:23], v[20:21], off
	s_cmp_lg_u32 s82, 0
	s_cbranch_scc0 .Le2_skip
	s_waitcnt vmcnt(7)
	v_cvt_scalef32_pk_fp8_f32 v250, v218, v222, v254
	v_cvt_scalef32_pk_fp8_f32 v251, v234, v238, v254
	v_cvt_scalef32_pk_fp8_f32 v250, v226, v230, v254 op_sel:[0,0,0,1]
	v_cvt_scalef32_pk_fp8_f32 v251, v242, v246, v254 op_sel:[0,0,0,1]
	global_store_dwordx2 v253, v[250:251], s[90:91] nt
	v_cvt_scalef32_pk_fp8_f32 v250, v219, v223, v254
	v_cvt_scalef32_pk_fp8_f32 v251, v235, v239, v254
	v_cvt_scalef32_pk_fp8_f32 v250, v227, v231, v254 op_sel:[0,0,0,1]
	v_cvt_scalef32_pk_fp8_f32 v251, v243, v247, v254 op_sel:[0,0,0,1]
	global_store_dwordx2 v253, v[250:251], s[90:91] offset:2048 nt
	v_cvt_scalef32_pk_fp8_f32 v250, v220, v224, v254
	v_cvt_scalef32_pk_fp8_f32 v251, v236, v240, v254
	v_cvt_scalef32_pk_fp8_f32 v250, v228, v232, v254 op_sel:[0,0,0,1]
	v_cvt_scalef32_pk_fp8_f32 v251, v244, v248, v254 op_sel:[0,0,0,1]
	s_add_u32 s90, s90, 0x1000
	s_addc_u32 s91, s91, 0
	global_store_dwordx2 v253, v[250:251], s[90:91] nt
	v_cvt_scalef32_pk_fp8_f32 v250, v221, v225, v254
	v_cvt_scalef32_pk_fp8_f32 v251, v237, v241, v254
	v_cvt_scalef32_pk_fp8_f32 v250, v229, v233, v254 op_sel:[0,0,0,1]
	v_cvt_scalef32_pk_fp8_f32 v251, v245, v249, v254 op_sel:[0,0,0,1]
	global_store_dwordx2 v253, v[250:251], s[90:91] offset:2048 nt
	s_add_i32 s98, s98, 1
	s_lshr_b32 s90, s98, 1
	s_mul_i32 s90, s90, s83
	s_add_i32 s90, s90, s84
	s_cmp_lt_u32 s90, 0x8000
	s_cbranch_scc0 .Le2_no
	s_lshr_b32 s91, s90, 10
	s_lshl_b32 s91, s91, 11
	s_and_b32 s99, s90, 0x3c0
	s_lshl_b32 s99, s99, 1
	s_or_b32 s91, s91, s99
	s_and_b32 s99, s98, 1
	s_lshl_b32 s99, s99, 6
	s_or_b32 s91, s91, s99
	s_and_b32 s90, s90, 63
	s_or_b32 s90, s90, s91
	s_lshr_b32 s91, s90, 11
	s_and_b32 s99, s90, 0x7c0
	s_and_b32 s82, s90, 63
	s_lshl_b32 s32, s91, 24
	s_lshl_b32 s100, s99, 13
	s_add_i32 s32, s32, s100
	s_lshl_b32 s100, s82, 7
	s_add_i32 s32, s32, s100
	s_add_u32 s100, s86, s32
	s_addc_u32 s101, s87, 0
	s_lshl_b32 s32, s91, 22
	s_lshl_b32 s82, s82, 16
	s_add_i32 s32, s32, s82
	s_add_i32 s32, s32, s99
	s_add_u32 s90, s88, s32
	s_addc_u32 s91, s89, 0
	global_load_dwordx4 v[218:221], v252, s[100:101] nt
	s_add_u32 s100, s100, 0x2000
	s_addc_u32 s101, s101, 0
	global_load_dwordx4 v[222:225], v252, s[100:101] nt
	s_add_u32 s100, s100, 0x2000
	s_addc_u32 s101, s101, 0
	global_load_dwordx4 v[226:229], v252, s[100:101] nt
	s_add_u32 s100, s100, 0x2000
	s_addc_u32 s101, s101, 0
	global_load_dwordx4 v[230:233], v252, s[100:101] nt
	s_add_u32 s100, s100, 0x2000
	s_addc_u32 s101, s101, 0
	global_load_dwordx4 v[234:237], v252, s[100:101] nt
	s_add_u32 s100, s100, 0x2000
	s_addc_u32 s101, s101, 0
	global_load_dwordx4 v[238:241], v252, s[100:101] nt
	s_add_u32 s100, s100, 0x2000
	s_addc_u32 s101, s101, 0
	global_load_dwordx4 v[242:245], v252, s[100:101] nt
	s_add_u32 s100, s100, 0x2000
	s_addc_u32 s101, s101, 0
	global_load_dwordx4 v[246:249], v252, s[100:101] nt
	s_mov_b32 s82, 2
	s_branch .Le2_skip

; __device__ __forceinline__ unsigned pk4_fp8(float a, float b, float c, float d) { int p = __builtin_amdgcn_cvt_pk_fp8_f32(a, b, 0, false); p = __builtin_amdgcn_cvt_pk_fp8_f32(c, d, p, true); return (unsigned)p; }
;     __device__ __forceinline__ void operator()(const f32x4 (&acc)[2][2][4][2], const Unit& u, int wr, int wc, int fr, int fq) const {
;     ...
;         for (int ai = 0; ai < 2; ++ai)
; #pragma unroll
;             for (int m = 0; m < 4; ++m) { float r[8];
; #pragma unroll
;                 for (int n = 0; n < 2; ++n)
; #pragma unroll
;                     for (int j = 0; j < 4; ++j) {
;                         float g = acc[ai][0][m][n][j] * W8_INV + bg[n][j], uu = acc[ai][1][m][n][j] * W8_INV + bu[n][j];
;                         g = fminf(g, 7.0f); uu = fminf(fmaxf(uu, -7.0f), 7.0f);
;                         const float glu = g * __builtin_amdgcn_rcpf(1.0f + __expf(-1.702f * g));
;                         r[n * 4 + j] = (uu + 1.0f) * glu; }
;                 u32x2 w; w.x = pk4_fp8(r[0], r[1], r[2], r[3]); w.y = pk4_fp8(r[4], r[5], r[6], r[7]);
;                 *(u32x2*)(O + (size_t)(row0 + ai * HALF + m * 16) * DM + cc) = w; }
.Le2_skip:
	v_mul_f32_e32 v21, 0xbfd9db23, v15
	v_add_f32_e32 v20, 1.0, v24
	v_mul_f32_e32 v21, 0x3fb8aa3b, v21
	v_rcp_f32_e32 v20, v20
	v_exp_f32_e32 v21, v21
	v_fmamk_f32 v10, v58, 0x3c800000, v10
	v_med3_f32 v10, v10, s57, v196
	v_mul_f32_e32 v14, v14, v20
	v_add_f32_e32 v20, 1.0, v21
	v_rcp_f32_e32 v20, v20
	v_add_f32_e32 v10, 1.0, v10
	v_mul_f32_e32 v10, v10, v14
	v_fmamk_f32 v11, v59, 0x3c800000, v11
	v_mul_f32_e32 v14, v15, v20
	v_fmamk_f32 v15, v64, 0x3c800000, v16
	v_min_f32_e32 v15, 0x40e00000, v15
	v_mul_f32_e32 v16, 0xbfd9db23, v15
	v_mul_f32_e32 v16, 0x3fb8aa3b, v16
	v_exp_f32_e32 v16, v16
	v_med3_f32 v11, v11, s57, v196
	v_add_f32_e32 v11, 1.0, v11
	v_fmac_f32_e32 v17, 0x3c800000, v65
	v_mul_f32_e32 v11, v11, v14
	v_add_f32_e32 v14, 1.0, v16
	v_min_f32_e32 v16, 0x40e00000, v17
	v_mul_f32_e32 v17, 0xbfd9db23, v16
	v_mul_f32_e32 v17, 0x3fb8aa3b, v17
	v_rcp_f32_e32 v14, v14
	v_exp_f32_e32 v17, v17
	v_fmamk_f32 v12, v60, 0x3c800000, v12
	v_med3_f32 v12, v12, s57, v196
	v_mul_f32_e32 v14, v15, v14
	v_add_f32_e32 v15, 1.0, v17
	v_rcp_f32_e32 v15, v15
	v_fmamk_f32 v6, v54, 0x3c800000, v6
	v_add_f32_e32 v12, 1.0, v12
	v_min_f32_e32 v6, 0x40e00000, v6
	v_mul_f32_e32 v12, v12, v14
	v_mul_f32_e32 v14, v16, v15
	v_mul_f32_e32 v15, 0xbfd9db23, v6
	v_mul_f32_e32 v15, 0x3fb8aa3b, v15
	v_exp_f32_e32 v15, v15
	v_fmac_f32_e32 v13, 0x3c800000, v61
	v_med3_f32 v13, v13, s57, v196
	v_fmamk_f32 v7, v55, 0x3c800000, v7
	v_add_f32_e32 v13, 1.0, v13
	v_min_f32_e32 v7, 0x40e00000, v7
	v_mul_f32_e32 v13, v13, v14
	v_add_f32_e32 v14, 1.0, v15
	v_mul_f32_e32 v15, 0xbfd9db23, v7
	v_mul_f32_e32 v15, 0x3fb8aa3b, v15
	v_rcp_f32_e32 v14, v14
	v_exp_f32_e32 v15, v15
	v_fmamk_f32 v2, v50, 0x3c800000, v2
	v_med3_f32 v2, v2, s57, v196
	v_mul_f32_e32 v6, v6, v14
	v_add_f32_e32 v14, 1.0, v15
	v_rcp_f32_e32 v14, v14
	v_add_f32_e32 v2, 1.0, v2
	v_mul_f32_e32 v6, v2, v6
	v_fmamk_f32 v2, v51, 0x3c800000, v3
	v_mul_f32_e32 v3, v7, v14
	v_fmamk_f32 v7, v56, 0x3c800000, v8
	v_min_f32_e32 v7, 0x40e00000, v7
	v_mul_f32_e32 v8, 0xbfd9db23, v7
	v_mul_f32_e32 v8, 0x3fb8aa3b, v8
	v_exp_f32_e32 v8, v8
	v_med3_f32 v2, v2, s57, v196
	v_add_f32_e32 v2, 1.0, v2
	v_fmac_f32_e32 v9, 0x3c800000, v57
	v_mul_f32_e32 v14, v2, v3
	v_fmamk_f32 v2, v52, 0x3c800000, v4
	v_min_f32_e32 v4, 0x40e00000, v9
	v_add_f32_e32 v3, 1.0, v8
	v_mul_f32_e32 v8, 0xbfd9db23, v4
	v_mul_f32_e32 v8, 0x3fb8aa3b, v8
	v_rcp_f32_e32 v3, v3
	v_exp_f32_e32 v8, v8
	v_med3_f32 v2, v2, s57, v196
	v_add_f32_e32 v2, 1.0, v2
	v_mul_f32_e32 v3, v7, v3
	v_add_f32_e32 v7, 1.0, v8
	v_rcp_f32_e32 v7, v7
	v_mul_f32_e32 v8, v2, v3
	v_mov_b32_e32 v2, v181
	v_mov_b32_e32 v3, v181
	v_fmac_f32_e32 v5, 0x3c800000, v53
	v_cvt_pk_fp8_f32 v2, v10, v11
	v_cvt_pk_fp8_f32 v3, v6, v14
	v_med3_f32 v5, v5, s57, v196
	v_mul_f32_e32 v4, v4, v7
	v_add_f32_e32 v5, 1.0, v5
	v_mul_f32_e32 v4, v5, v4
	v_cvt_pk_fp8_f32 v2, v12, v13 op_sel:[0,0,1]
	v_cvt_pk_fp8_f32 v3, v8, v4 op_sel:[0,0,1]
	v_add_co_u32_e32 v4, vcc, 0x58000, v18
	s_nop 1
	v_addc_co_u32_e32 v5, vcc, 0, v19, vcc
	s_and_b64 vcc, exec, s[22:23]
	global_store_dwordx2 v[4:5], v[2:3], off
	s_cbranch_vccnz .LBB0_871
